# baseline (speedup 1.0000x reference)
.Lh_no_out:
	s_cmp_eq_u32 s17, 0
	s_cselect_b32 s4, s4, s6
	s_cselect_b32 s5, s5, s7
	s_add_u32 s24, s8, s22
	s_addc_u32 s25, s9, 0
	s_add_u32 s4, s4, s21
	s_addc_u32 s5, s5, 0
	global_load_dwordx4 v[14:17], v18, s[24:25] nt
	global_load_dwordx4 v[2:5], v18, s[4:5] nt
	s_add_u32 s6, s4, 0x40000
	s_addc_u32 s7, s5, 0
	s_add_u32 s8, s4, 0x80000
	s_addc_u32 s9, s5, 0
	s_barrier
	global_load_dwordx4 v[6:9], v18, s[6:7] nt
	s_barrier
	global_load_dwordx4 v[10:13], v18, s[8:9] nt
	s_mul_i32 s46, s3, 0xc00
	s_add_u32 s46, s46, 0x8420
	v_lshl_add_u32 v26, v1, 2, s46
	v_and_b32_e32 v38, 15, v0
	s_mul_i32 s58, s17, 0x4200
	s_add_u32 s58, s58, 0x1e0
	v_lshl_add_u32 v38, v38, 2, s58
	v_add_u32_e32 v39, 0x1600, v38
	v_add_u32_e32 v40, 0x2c00, v38
	v_mov_b32_e32 v41, 0x41fc0000
	v_mov_b32_e32 v42, 0xbf38aa3b
	s_mov_b32 s48, 0x3f940000
	s_mov_b32 s51, 0x3fb8aa3b
	s_mov_b32 s60, 0x3ebc5ab2
	s_mov_b32 s61, 0xbf38aa3b
	s_mov_b32 s42, 0
	s_mov_b32 s43, 0
	s_mov_b32 s44, 0x7fffffff
	s_mov_b32 s45, 0x7fffffff
	s_mov_b32 s47, 0
	s_mul_i32 s58, s3, 0x1600
	s_add_u32 s58, s58, 0x320
	v_lshl_add_u32 v44, v1, 6, s58
	v_bfe_u32 v45, v1, 2, 2
	v_lshlrev_b32_e32 v45, 4, v45
	v_xor_b32_e32 v46, 16, v45
	v_xor_b32_e32 v47, 32, v45
	v_xor_b32_e32 v48, 48, v45
	v_add_u32_e32 v45, v44, v45
	v_add_u32_e32 v46, v44, v46
	v_add_u32_e32 v47, v44, v47
	v_add_u32_e32 v48, v44, v48
	s_mul_i32 s58, s2, 0x600
	s_lshl_b32 s59, s3, 8
	s_add_u32 s58, s58, s59
	s_add_u32 s10, s10, s58
	s_addc_u32 s11, s11, 0
	v_lshlrev_b32_e32 v49, 2, v1
	s_lshl_b32 s58, s2, 2
	s_add_u32 s12, s12, s58
	s_addc_u32 s13, s13, 0
	s_setprio 3
	s_cmp_lt_u32 s3, 8
	s_cbranch_scc1 .Lh_nostagger
	s_sleep 3

.Lh_loop_body:
	v_fmamk_f32 v27, v24, 0x42000000, v41
	v_add_u32_e32 v26, 0x100, v26
	ds_read_b32 v24, v26
	s_sub_i32 s49, s44, s43
	s_sub_i32 s50, s45, s43
	s_add_i32 s43, s43, 64
	v_rndne_f32_e32 v28, v27
	v_cmp_le_i32_e32 vcc, s49, v1
	v_cmp_le_i32_e64 s[52:53], s50, v1
	v_sub_f32_e32 v29, v27, v28
	v_cvt_i32_f32_e32 v30, v28
	v_cndmask_b32_e32 v36, v38, v39, vcc
	v_mul_f32_e32 v37, s61, v29
	v_cndmask_b32_e64 v36, v36, v40, s[52:53]
	v_fmamk_f32 v32, v29, 0x3fb8aa3b, v42
	v_fma_f32 v33, -v29, s51, v42
	v_fmaak_f32 v31, v29, v37, 0x41a00000
	v_lshl_add_u32 v30, v30, 6, v36
	v_exp_f32_e32 v31, v31
	v_exp_f32_e32 v32, v32
	v_exp_f32_e32 v33, v33
	v_cvt_rpi_i32_f32_e32 v36, v31
	ds_add_u32 v30, v36 offset:320
	v_mul_f32_e32 v34, v32, v31
	v_mul_f32_e32 v35, v33, v31
	v_cvt_rpi_i32_f32_e32 v36, v34
	v_cvt_rpi_i32_f32_e32 v37, v35
	ds_add_u32 v30, v36 offset:384
	ds_add_u32 v30, v37 offset:256
	v_mul_f32_e32 v32, s60, v32
	v_mul_f32_e32 v33, s60, v33
	v_mul_f32_e32 v34, v32, v34
	v_mul_f32_e32 v35, v33, v35
	v_cvt_rpi_i32_f32_e32 v36, v34
	v_cvt_rpi_i32_f32_e32 v37, v35
	ds_add_u32 v30, v36 offset:448
	ds_add_u32 v30, v37 offset:192
	v_mul_f32_e32 v32, s60, v32
	v_mul_f32_e32 v33, s60, v33
	v_mul_f32_e32 v34, v32, v34
	v_mul_f32_e32 v35, v33, v35
	v_cvt_rpi_i32_f32_e32 v36, v34
	v_cvt_rpi_i32_f32_e32 v37, v35
	ds_add_u32 v30, v36 offset:512
	ds_add_u32 v30, v37 offset:128
	v_mul_f32_e32 v32, s60, v32
	v_mul_f32_e32 v33, s60, v33
	v_mul_f32_e32 v34, v32, v34
	v_mul_f32_e32 v35, v33, v35
	v_cvt_rpi_i32_f32_e32 v36, v34
	v_cvt_rpi_i32_f32_e32 v37, v35
	ds_add_u32 v30, v36 offset:576
	ds_add_u32 v30, v37 offset:64
	v_mul_f32_e32 v32, s60, v32
	v_mul_f32_e32 v33, s60, v33
	v_mul_f32_e32 v34, v32, v34
	v_mul_f32_e32 v35, v33, v35
	v_cvt_rpi_i32_f32_e32 v36, v34
	v_cvt_rpi_i32_f32_e32 v37, v35
	ds_add_u32 v30, v36 offset:640
	ds_add_u32 v30, v37
	s_sub_i32 s59, s42, s43
	s_cmp_ge_i32 s59, 64
	s_waitcnt lgkmcnt(11)
	s_cbranch_scc1 .Lh_loop_body

	.amdhsa_kernel _Z6k_histPKfS0_S0_PfPiS1_
		.amdhsa_group_segment_fixed_size 32
		.amdhsa_private_segment_fixed_size 0
		.amdhsa_kernarg_size 48
		.amdhsa_user_sgpr_count 2
		.amdhsa_user_sgpr_dispatch_ptr 0
		.amdhsa_user_sgpr_queue_ptr 0
		.amdhsa_user_sgpr_kernarg_segment_ptr 1
		.amdhsa_user_sgpr_dispatch_id 0
		.amdhsa_user_sgpr_kernarg_preload_length 0
		.amdhsa_user_sgpr_kernarg_preload_offset 0
		.amdhsa_user_sgpr_private_segment_size 0
		.amdhsa_uses_dynamic_stack 0
		.amdhsa_enable_private_segment 0
		.amdhsa_system_sgpr_workgroup_id_x 1
		.amdhsa_system_sgpr_workgroup_id_y 0
		.amdhsa_system_sgpr_workgroup_id_z 0
		.amdhsa_system_sgpr_workgroup_info 0
		.amdhsa_system_vgpr_workitem_id 0
		.amdhsa_next_free_vgpr 50
		.amdhsa_next_free_sgpr 62
		.amdhsa_accum_offset 52
		.amdhsa_reserve_vcc 1
		.amdhsa_float_round_mode_32 0
		.amdhsa_float_round_mode_16_64 0
		.amdhsa_float_denorm_mode_32 3
		.amdhsa_float_denorm_mode_16_64 3
		.amdhsa_dx10_clamp 1
		.amdhsa_ieee_mode 1
		.amdhsa_fp16_overflow 0
		.amdhsa_tg_split 0
		.amdhsa_exception_fp_ieee_invalid_op 0
		.amdhsa_exception_fp_denorm_src 0
		.amdhsa_exception_fp_ieee_div_zero 0
		.amdhsa_exception_fp_ieee_overflow 0
		.amdhsa_exception_fp_ieee_underflow 0
		.amdhsa_exception_fp_ieee_inexact 0
		.amdhsa_exception_int_div_zero 0
	.end_amdhsa_kernel

.Lfunc_end0:
	.size	_Z6k_histPKfS0_S0_PfPiS1_, .Lfunc_end0-_Z6k_histPKfS0_S0_PfPiS1_
	.set _Z6k_histPKfS0_S0_PfPiS1_.num_vgpr, 50
	.set _Z6k_histPKfS0_S0_PfPiS1_.num_agpr, 0
	.set _Z6k_histPKfS0_S0_PfPiS1_.numbered_sgpr, 62
	.set _Z6k_histPKfS0_S0_PfPiS1_.num_named_barrier, 0
	.set _Z6k_histPKfS0_S0_PfPiS1_.private_seg_size, 0
	.set _Z6k_histPKfS0_S0_PfPiS1_.uses_vcc, 1
	.set _Z6k_histPKfS0_S0_PfPiS1_.uses_flat_scratch, 0
	.set _Z6k_histPKfS0_S0_PfPiS1_.has_dyn_sized_stack, 0
	.set _Z6k_histPKfS0_S0_PfPiS1_.has_recursion, 0
	.set _Z6k_histPKfS0_S0_PfPiS1_.has_indirect_call, 0

amdhsa.kernels:
  - .agpr_count:     0
    .args:
      - .actual_access:  read_only
        .address_space:  global
        .offset:         0
        .size:           8
        .value_kind:     global_buffer
      - .actual_access:  read_only
        .address_space:  global
        .offset:         8
        .size:           8
        .value_kind:     global_buffer
      - .actual_access:  read_only
        .address_space:  global
        .offset:         16
        .size:           8
        .value_kind:     global_buffer
      - .actual_access:  write_only
        .address_space:  global
        .offset:         24
        .size:           8
        .value_kind:     global_buffer
      - .actual_access:  write_only
        .address_space:  global
        .offset:         32
        .size:           8
        .value_kind:     global_buffer
      - .actual_access:  write_only
        .address_space:  global
        .offset:         40
        .size:           8
        .value_kind:     global_buffer
    .group_segment_fixed_size: 32
    .kernarg_segment_align: 8
    .kernarg_segment_size: 48
    .language:       OpenCL C
    .language_version:
      - 2
      - 0
    .max_flat_workgroup_size: 1024
    .name:           _Z6k_histPKfS0_S0_PfPiS1_
    .private_segment_fixed_size: 0
    .sgpr_count:     68
    .sgpr_spill_count: 0
    .symbol:         _Z6k_histPKfS0_S0_PfPiS1_.kd
    .uniform_work_group_size: 1
    .uses_dynamic_stack: false
    .vgpr_count:     50
    .vgpr_spill_count: 0
    .wavefront_size: 64
  - .agpr_count:     0
    .args:
      - .actual_access:  read_only
        .address_space:  global
        .offset:         0
        .size:           8
        .value_kind:     global_buffer
      - .actual_access:  read_only
        .address_space:  global
        .offset:         8
        .size:           8
        .value_kind:     global_buffer
      - .address_space:  global
        .offset:         16
        .size:           8
        .value_kind:     global_buffer
    .group_segment_fixed_size: 2080
    .kernarg_segment_align: 8
    .kernarg_segment_size: 24
    .language:       OpenCL C
    .language_version:
      - 2
      - 0
    .max_flat_workgroup_size: 256
    .name:           _Z7k_finalPKfPKiPf
    .private_segment_fixed_size: 0
    .sgpr_count:     34
    .sgpr_spill_count: 0
    .symbol:         _Z7k_finalPKfPKiPf.kd
    .uniform_work_group_size: 1
    .uses_dynamic_stack: false
    .vgpr_count:     36
    .vgpr_spill_count: 0
    .wavefront_size: 64
